# speedup vs baseline: 1.0046x; 1.0046x over previous
_Z14attn_bh_kernelPKDF16_S0_S0_PDF16_i:
	s_load_dwordx4 s[8:11], s[0:1], 0x0
	s_load_dwordx2 s[4:5], s[0:1], 0x10
	s_load_dword s3, s[0:1], 0x20
	v_lshrrev_b32_e32 v2, 6, v0
	v_and_b32_e32 v86, 31, v0
	s_lshr_b32 s6, s2, 3
	s_mul_i32 s12, s6, 0x248
	s_waitcnt lgkmcnt(0)
	v_add_u32_e32 v87, s3, v2
	s_mov_b32 s25, s3
	v_lshl_or_b32 v2, v87, 5, v86
	v_min_i32_e32 v2, 0x247, v2
	v_add_u32_e32 v2, s12, v2
	v_ashrrev_i32_e32 v3, 31, v2
	s_lshl_b32 s3, s2, 6
	v_lshlrev_b64 v[2:3], 10, v[2:3]
	s_and_b32 s14, s3, 0x1c0
	v_bfe_u32 v1, v0, 5, 1
	v_lshl_add_u64 v[2:3], s[8:9], 0, v[2:3]
	s_mov_b32 s7, 0
	s_lshl_b32 s6, s14, 1
	v_mov_b32_e32 v45, 0
	v_lshl_add_u64 v[2:3], v[2:3], 0, s[6:7]
	v_lshlrev_b32_e32 v42, 4, v1
	v_mov_b32_e32 v43, v45
	s_mul_hi_i32 s3, s2, 0x12400
	s_mul_i32 s2, s2, 0x12400
	v_lshl_add_u64 v[2:3], v[2:3], 0, v[42:43]
	s_add_u32 s2, s4, s2
	global_load_dwordx4 v[66:69], v[2:3], off
	global_load_dwordx4 v[70:73], v[2:3], off offset:32
	global_load_dwordx4 v[74:77], v[2:3], off offset:64
	global_load_dwordx4 v[78:81], v[2:3], off offset:96
	s_addc_u32 s3, s5, s3
	s_ashr_i32 s13, s12, 31
	s_lshl_b64 s[16:17], s[12:13], 10
	s_add_u32 s16, s10, s16
	s_addc_u32 s17, s11, s17
	s_add_u32 s16, s16, s6
	s_addc_u32 s17, s17, 0
	v_lshrrev_b32_e32 v4, 6, v0
	v_and_b32_e32 v5, 63, v0
	v_lshrrev_b32_e32 v6, 3, v5
	v_readfirstlane_b32 s15, v4
	v_and_b32_e32 v7, 7, v5
	s_movk_i32 s23, 0x400
	s_movk_i32 s24, 0x490
	s_mov_b32 s19, 0x10000
	s_movk_i32 s20, 0x80
	s_and_b32 s18, s15, 7
	s_lshl_b32 s21, s18, 3
	s_lshl_b32 s18, s18, 10
	v_add_u32_e32 v9, s21, v6
	s_cmp_lt_u32 s15, 8
	s_cselect_b32 s23, s23, s24
	s_cselect_b32 s21, s19, s20
	s_cselect_b32 s16, s16, s2
	s_cselect_b32 s17, s17, s3
	s_cselect_b32 s24, 0, 0x12400
	s_add_u32 s18, s18, s24
	v_bfe_u32 v10, v9, 1, 3
	v_xor_b32_e32 v10, v10, v7
	v_mul_u32_u24_e32 v8, s23, v9
	v_lshl_add_u32 v8, v10, 4, v8
	s_mov_b32 m0, s18
	s_add_u32 s18, s18, 0x2000
	global_load_lds_dwordx4 v8, s[16:17]
	v_add_u32_e32 v8, s21, v8
	s_cmp_lg_u32 s15, 0
	s_cbranch_scc1 .Lat_nw0
	v_add_u32_e32 v11, 0x80000, v8
	s_mov_b32 m0, 0x12000
	s_nop 0
	global_load_lds_dwordx4 v11, s[16:17]

.Lat_nw8:
	s_mov_b32 m0, s18
	s_add_u32 s18, s18, 0x2000
	global_load_lds_dwordx4 v8, s[16:17]
	v_add_u32_e32 v8, s21, v8
	s_waitcnt vmcnt(1)
	s_cmp_lt_u32 s15, 8
	s_cbranch_scc1 .Lat_nt9
	s_sub_u32 s24, s15, 8
	v_bfe_u32 v16, v5, 1, 3
	v_xor_b32_e32 v16, s24, v16
	v_lshlrev_b32_e32 v17, 7, v5
	v_lshl_add_u32 v16, v16, 4, v17
	v_add_u32_e32 v16, 0x24400, v16
	s_cmp_eq_u32 s15, 8
	s_cbranch_scc1 .Lat_t9d
	v_mov_b32_e32 v12, 0
	v_mov_b32_e32 v13, 0
	v_mov_b32_e32 v14, 0
	v_mov_b32_e32 v15, 0

.Lat_nt9:
	v_and_b32_e32 v2, 19, v0
	v_lshlrev_b32_e32 v3, 1, v0
	v_lshrrev_b32_e32 v0, 1, v0
	v_and_b32_e32 v3, 8, v3
	v_and_b32_e32 v0, 4, v0
	v_or3_b32 v0, v3, v2, v0
	v_lshrrev_b32_e32 v2, 1, v0
	v_bfe_u32 v3, v0, 1, 3
	v_lshlrev_b32_e32 v0, 7, v0
	v_bitop3_b32 v2, v1, v2, 7 bitop3:0x78
	v_lshl_add_u32 v88, v2, 4, v0
	v_bitop3_b32 v2, v1, v3, 2 bitop3:0x36
	v_lshl_add_u32 v89, v2, 4, v0
	v_bitop3_b32 v2, v1, v3, 4 bitop3:0x36
	v_lshl_add_u32 v90, v2, 4, v0
	v_bitop3_b32 v2, v1, v3, 6 bitop3:0x36
	v_lshl_add_u32 v91, v2, 4, v0
	v_bfe_u32 v3, v86, 1, 3
	v_lshlrev_b32_e32 v2, 7, v86
	v_add_u32_e32 v2, 0x12400, v2
	v_xor_b32_e32 v4, v1, v3
	v_lshl_add_u32 v93, v4, 4, v2
	v_or_b32_e32 v4, 2, v1
	v_xor_b32_e32 v4, v4, v3
	v_lshl_add_u32 v114, v4, 4, v2
	v_or_b32_e32 v4, 4, v1
	v_xor_b32_e32 v4, v4, v3
	v_lshl_add_u32 v115, v4, 4, v2
	v_or_b32_e32 v4, 6, v1
	v_xor_b32_e32 v4, v4, v3
	v_lshl_add_u32 v116, v4, 4, v2
	s_mov_b32 s22, 64
	s_mov_b64 s[26:27], s[16:17]
	s_mov_b32 s23, s18
	s_mov_b32 s24, s21
	v_mov_b32_e32 v120, v8
	v_cmp_gt_i32_e32 vcc, 19, v87
	s_waitcnt lgkmcnt(0)
	s_barrier
	s_cmp_lg_u32 s25, 0
	s_cbranch_scc1 .Lat_nopre
	s_mov_b32 m0, s23
	s_add_u32 s23, s23, 0x2000
	global_load_lds_dwordx4 v120, s[26:27]
	v_add_u32_e32 v120, s24, v120
	s_mov_b32 m0, s23
	s_add_u32 s23, s23, 0x2000
	global_load_lds_dwordx4 v120, s[26:27]
	v_add_u32_e32 v120, s24, v120
	s_mov_b32 m0, s23
	s_add_u32 s23, s23, 0x2000
	global_load_lds_dwordx4 v120, s[26:27]
	v_add_u32_e32 v120, s24, v120
	s_mov_b32 m0, s23
	s_add_u32 s23, s23, 0x2000
	global_load_lds_dwordx4 v120, s[26:27]
	v_add_u32_e32 v120, s24, v120
	s_mov_b32 m0, s23
	s_add_u32 s23, s23, 0x2000
	global_load_lds_dwordx4 v120, s[26:27]
	v_add_u32_e32 v120, s24, v120
	s_mov_b32 m0, s23
	s_add_u32 s23, s23, 0x2000
	global_load_lds_dwordx4 v120, s[26:27]
	v_add_u32_e32 v120, s24, v120
	s_mov_b32 m0, s23
	s_add_u32 s23, s23, 0x2000
	global_load_lds_dwordx4 v120, s[26:27]
	v_add_u32_e32 v120, s24, v120
.Lat_nopre:
	s_and_saveexec_b64 s[2:3], vcc
	s_cbranch_execz .Lat_notile
	s_load_dwordx2 s[4:5], s[0:1], 0x18
	v_lshlrev_b32_e32 v92, 3, v1
	s_add_u32 s0, s8, s6
	v_mov_b32_e32 v0, 0
	s_addc_u32 s1, s9, 0
	v_lshlrev_b32_e32 v2, 1, v92
	v_mov_b32_e32 v3, v0
	v_or_b32_e32 v1, s14, v92
	v_lshl_add_u64 v[82:83], s[0:1], 0, v[2:3]
	s_mov_b32 s7, 0x20000
	s_brev_b32 s6, -2
	s_waitcnt lgkmcnt(0)
	s_and_b32 s5, s5, 0xffff
	s_mov_b64 s[2:3], 0
	s_movk_i32 s13, 0x248
	v_mov_b32_e32 v94, 0x247
	s_movk_i32 s18, 0x205
	s_mov_b32 s19, 0x41000000
	s_mov_b32 s20, 0xc1000000
	v_lshlrev_b32_e32 v95, 1, v1
	v_mov_b32_e32 v96, 0xf149f2ca
	v_mov_b32_e32 v97, v87
	s_branch .LBB2_9

.LBB2_14:
	s_cmp_eq_u32 s22, -1
	s_cbranch_scc1 .Lat_qkA
	s_cmp_eq_u32 s21, s22
	s_cbranch_scc0 .Lat_qkB
	s_cmp_eq_u32 s25, 0
	s_cbranch_scc1 .Lat_fin
	s_cmp_eq_u32 s22, 64
	s_cbranch_scc1 .Lat_t1
	s_cmp_eq_u32 s22, 0x80
	s_cbranch_scc1 .Lat_t2
	s_cmp_eq_u32 s22, 0xc0
	s_cbranch_scc1 .Lat_t3
.Lat_fin:
	s_waitcnt vmcnt(0)
	s_barrier
	s_mov_b32 s22, -1
	s_branch .Lat_qkA
.Lat_t1:
	s_mov_b32 m0, s23
	s_add_u32 s23, s23, 0x2000
	global_load_lds_dwordx4 v120, s[26:27]
	v_add_u32_e32 v120, s24, v120
	s_mov_b32 m0, s23
	s_add_u32 s23, s23, 0x2000
	global_load_lds_dwordx4 v120, s[26:27]
	v_add_u32_e32 v120, s24, v120
	s_waitcnt vmcnt(2)
	s_barrier
	s_movk_i32 s22, 0x80
	s_branch .Lat_qkB
.Lat_t2:
	s_mov_b32 m0, s23
	s_add_u32 s23, s23, 0x2000
	global_load_lds_dwordx4 v120, s[26:27]
	v_add_u32_e32 v120, s24, v120
	s_mov_b32 m0, s23
	s_add_u32 s23, s23, 0x2000
	global_load_lds_dwordx4 v120, s[26:27]
	v_add_u32_e32 v120, s24, v120
	s_waitcnt vmcnt(3)
	s_barrier
	s_movk_i32 s22, 0xc0
	s_branch .Lat_qkB
.Lat_t3:
	s_mov_b32 m0, s23
	s_add_u32 s23, s23, 0x2000
	global_load_lds_dwordx4 v120, s[26:27]
	v_add_u32_e32 v120, s24, v120
	s_mov_b32 m0, s23
	s_add_u32 s23, s23, 0x2000
	global_load_lds_dwordx4 v120, s[26:27]
	v_add_u32_e32 v120, s24, v120
	s_mov_b32 m0, s23
	s_add_u32 s23, s23, 0x2000
	global_load_lds_dwordx4 v120, s[26:27]
	v_add_u32_e32 v120, s24, v120
	s_waitcnt vmcnt(5)
	s_barrier
	s_movk_i32 s22, 0x100

.Lat_notile:
	s_mov_b64 exec, -1
	s_mov_b32 m0, s23
	s_add_u32 s23, s23, 0x2000
	global_load_lds_dwordx4 v120, s[26:27]
	v_add_u32_e32 v120, s24, v120
	s_mov_b32 m0, s23
	s_add_u32 s23, s23, 0x2000
	global_load_lds_dwordx4 v120, s[26:27]
	v_add_u32_e32 v120, s24, v120
	s_waitcnt vmcnt(2)
	s_barrier
	s_mov_b32 m0, s23
	s_add_u32 s23, s23, 0x2000
	global_load_lds_dwordx4 v120, s[26:27]
	v_add_u32_e32 v120, s24, v120
	s_mov_b32 m0, s23
	s_add_u32 s23, s23, 0x2000
	global_load_lds_dwordx4 v120, s[26:27]
	v_add_u32_e32 v120, s24, v120
	s_waitcnt vmcnt(3)
	s_barrier
	s_mov_b32 m0, s23
	s_add_u32 s23, s23, 0x2000
	global_load_lds_dwordx4 v120, s[26:27]
	v_add_u32_e32 v120, s24, v120
	s_mov_b32 m0, s23
	s_add_u32 s23, s23, 0x2000
	global_load_lds_dwordx4 v120, s[26:27]
	v_add_u32_e32 v120, s24, v120
	s_mov_b32 m0, s23
	s_add_u32 s23, s23, 0x2000
	global_load_lds_dwordx4 v120, s[26:27]
	v_add_u32_e32 v120, s24, v120
	s_waitcnt vmcnt(5)
	s_barrier
	s_waitcnt vmcnt(0)
	s_barrier
	s_endpgm
	.p2align	8

	.amdhsa_kernel _Z14attn_bh_kernelPKDF16_S0_S0_PDF16_i
		.amdhsa_group_segment_fixed_size 0
		.amdhsa_private_segment_fixed_size 0
		.amdhsa_kernarg_size 36
		.amdhsa_user_sgpr_count 2
		.amdhsa_user_sgpr_dispatch_ptr 0
		.amdhsa_user_sgpr_queue_ptr 0
		.amdhsa_user_sgpr_kernarg_segment_ptr 1
		.amdhsa_user_sgpr_dispatch_id 0
		.amdhsa_user_sgpr_kernarg_preload_length 0
		.amdhsa_user_sgpr_kernarg_preload_offset 0
		.amdhsa_user_sgpr_private_segment_size 0
		.amdhsa_uses_dynamic_stack 0
		.amdhsa_enable_private_segment 0
		.amdhsa_system_sgpr_workgroup_id_x 1
		.amdhsa_system_sgpr_workgroup_id_y 0
		.amdhsa_system_sgpr_workgroup_id_z 0
		.amdhsa_system_sgpr_workgroup_info 0
		.amdhsa_system_vgpr_workitem_id 0
		.amdhsa_next_free_vgpr 121
		.amdhsa_next_free_sgpr 32
		.amdhsa_accum_offset 124
		.amdhsa_reserve_vcc 1
		.amdhsa_float_round_mode_32 0
		.amdhsa_float_round_mode_16_64 0
		.amdhsa_float_denorm_mode_32 3
		.amdhsa_float_denorm_mode_16_64 3
		.amdhsa_dx10_clamp 1
		.amdhsa_ieee_mode 1
		.amdhsa_fp16_overflow 0
		.amdhsa_tg_split 0
		.amdhsa_exception_fp_ieee_invalid_op 0
		.amdhsa_exception_fp_denorm_src 0
		.amdhsa_exception_fp_ieee_div_zero 0
		.amdhsa_exception_fp_ieee_overflow 0
		.amdhsa_exception_fp_ieee_underflow 0
		.amdhsa_exception_fp_ieee_inexact 0
		.amdhsa_exception_int_div_zero 0
	.end_amdhsa_kernel

amdhsa.kernels:
  - .agpr_count:     0
    .args:
      - .offset:         0
        .size:           136
        .value_kind:     by_value
      - .actual_access:  read_only
        .address_space:  global
        .offset:         136
        .size:           8
        .value_kind:     global_buffer
      - .actual_access:  read_only
        .address_space:  global
        .offset:         144
        .size:           8
        .value_kind:     global_buffer
      - .actual_access:  read_only
        .address_space:  global
        .offset:         152
        .size:           8
        .value_kind:     global_buffer
      - .actual_access:  read_only
        .address_space:  global
        .offset:         160
        .size:           8
        .value_kind:     global_buffer
      - .actual_access:  write_only
        .address_space:  global
        .offset:         168
        .size:           8
        .value_kind:     global_buffer
      - .actual_access:  write_only
        .address_space:  global
        .offset:         176
        .size:           8
        .value_kind:     global_buffer
    .group_segment_fixed_size: 0
    .kernarg_segment_align: 8
    .kernarg_segment_size: 184
    .language:       OpenCL C
    .language_version:
      - 2
      - 0
    .max_flat_workgroup_size: 256
    .name:           _Z15prologue_kernel8PrepArgsPKfS1_PKiS1_PDF16_Pf
    .private_segment_fixed_size: 0
    .sgpr_count:     36
    .sgpr_spill_count: 0
    .symbol:         _Z15prologue_kernel8PrepArgsPKfS1_PKiS1_PDF16_Pf.kd
    .uniform_work_group_size: 1
    .uses_dynamic_stack: false
    .vgpr_count:     44
    .vgpr_spill_count: 0
    .wavefront_size: 64
  - .agpr_count:     0
    .args:
      - .actual_access:  read_only
        .address_space:  global
        .offset:         0
        .size:           8
        .value_kind:     global_buffer
      - .offset:         8
        .size:           4
        .value_kind:     by_value
      - .offset:         12
        .size:           4
        .value_kind:     by_value
      - .actual_access:  read_only
        .address_space:  global
        .offset:         16
        .size:           8
        .value_kind:     global_buffer
      - .actual_access:  read_only
        .address_space:  global
        .offset:         24
        .size:           8
        .value_kind:     global_buffer
      - .actual_access:  read_only
        .address_space:  global
        .offset:         32
        .size:           8
        .value_kind:     global_buffer
      - .actual_access:  read_only
        .address_space:  global
        .offset:         40
        .size:           8
        .value_kind:     global_buffer
      - .address_space:  global
        .offset:         48
        .size:           8
        .value_kind:     global_buffer
      - .actual_access:  write_only
        .address_space:  global
        .offset:         56
        .size:           8
        .value_kind:     global_buffer
    .group_segment_fixed_size: 0
    .kernarg_segment_align: 8
    .kernarg_segment_size: 64
    .language:       OpenCL C
    .language_version:
      - 2
      - 0
    .max_flat_workgroup_size: 256
    .name:           _Z18ffn2_finish_kernelPKfiiS0_PK15HIP_vector_typeIfLj2EES0_S0_PDF16_PS2_
    .private_segment_fixed_size: 0
    .sgpr_count:     20
    .sgpr_spill_count: 0
    .symbol:         _Z18ffn2_finish_kernelPKfiiS0_PK15HIP_vector_typeIfLj2EES0_S0_PDF16_PS2_.kd
    .uniform_work_group_size: 1
    .uses_dynamic_stack: false
    .vgpr_count:     52
    .vgpr_spill_count: 0
    .wavefront_size: 64
  - .agpr_count:     0
    .args:
      - .actual_access:  read_only
        .address_space:  global
        .offset:         0
        .size:           8
        .value_kind:     global_buffer
      - .actual_access:  read_only
        .address_space:  global
        .offset:         8
        .size:           8
        .value_kind:     global_buffer
      - .actual_access:  read_only
        .address_space:  global
        .offset:         16
        .size:           8
        .value_kind:     global_buffer
      - .actual_access:  write_only
        .address_space:  global
        .offset:         24
        .size:           8
        .value_kind:     global_buffer
      - .offset:         32
        .size:           4
        .value_kind:     by_value
    .group_segment_fixed_size: 0
    .kernarg_segment_align: 8
    .kernarg_segment_size: 36
    .language:       OpenCL C
    .language_version:
      - 2
      - 0
    .max_flat_workgroup_size: 1024
    .name:           _Z14attn_bh_kernelPKDF16_S0_S0_PDF16_i
    .private_segment_fixed_size: 0
    .sgpr_count:     38
    .sgpr_spill_count: 0
    .symbol:         _Z14attn_bh_kernelPKDF16_S0_S0_PDF16_i.kd
    .uniform_work_group_size: 1
    .uses_dynamic_stack: false
    .vgpr_count:     121
    .vgpr_spill_count: 0
    .wavefront_size: 64
  - .agpr_count:     0
    .args:
      - .offset:         0
        .size:           336
        .value_kind:     by_value
    .group_segment_fixed_size: 0
    .kernarg_segment_align: 8
    .kernarg_segment_size: 336
    .language:       OpenCL C
    .language_version:
      - 2
      - 0
    .max_flat_workgroup_size: 256
    .name:           _Z11gemm_kernelILi0EEv8GemmArgs
    .private_segment_fixed_size: 0
    .sgpr_count:     47
    .sgpr_spill_count: 0
    .symbol:         _Z11gemm_kernelILi0EEv8GemmArgs.kd
    .uniform_work_group_size: 1
    .uses_dynamic_stack: false
    .vgpr_count:     198
    .vgpr_spill_count: 0
    .wavefront_size: 64
  - .agpr_count:     0
    .args:
      - .offset:         0
        .size:           336
        .value_kind:     by_value
    .group_segment_fixed_size: 0
    .kernarg_segment_align: 8
    .kernarg_segment_size: 336
    .language:       OpenCL C
    .language_version:
      - 2
      - 0
    .max_flat_workgroup_size: 256
    .name:           _Z11gemm_kernelILi1EEv8GemmArgs
    .private_segment_fixed_size: 0
    .sgpr_count:     43
    .sgpr_spill_count: 0
    .symbol:         _Z11gemm_kernelILi1EEv8GemmArgs.kd
    .uniform_work_group_size: 1
    .uses_dynamic_stack: false
    .vgpr_count:     202
    .vgpr_spill_count: 0
    .wavefront_size: 64
  - .agpr_count:     0
    .args:
      - .offset:         0
        .size:           336
        .value_kind:     by_value
    .group_segment_fixed_size: 0
    .kernarg_segment_align: 8
    .kernarg_segment_size: 336
    .language:       OpenCL C
    .language_version:
      - 2
      - 0
    .max_flat_workgroup_size: 256
    .name:           _Z11gemm_kernelILi2EEv8GemmArgs
    .private_segment_fixed_size: 0
    .sgpr_count:     41
    .sgpr_spill_count: 0
    .symbol:         _Z11gemm_kernelILi2EEv8GemmArgs.kd
    .uniform_work_group_size: 1
    .uses_dynamic_stack: false
    .vgpr_count:     198
    .vgpr_spill_count: 0
    .wavefront_size: 64
  - .agpr_count:     0
    .args:
      - .offset:         0
        .size:           336
        .value_kind:     by_value
      - .offset:         336
        .size:           4
        .value_kind:     hidden_block_count_x
      - .offset:         340
        .size:           4
        .value_kind:     hidden_block_count_y
      - .offset:         344
        .size:           4
        .value_kind:     hidden_block_count_z
      - .offset:         348
        .size:           2
        .value_kind:     hidden_group_size_x
      - .offset:         350
        .size:           2
        .value_kind:     hidden_group_size_y
      - .offset:         352
        .size:           2
        .value_kind:     hidden_group_size_z
      - .offset:         354
        .size:           2
        .value_kind:     hidden_remainder_x
      - .offset:         356
        .size:           2
        .value_kind:     hidden_remainder_y
      - .offset:         358
        .size:           2
        .value_kind:     hidden_remainder_z
      - .offset:         376
        .size:           8
        .value_kind:     hidden_global_offset_x
      - .offset:         384
        .size:           8
        .value_kind:     hidden_global_offset_y
      - .offset:         392
        .size:           8
        .value_kind:     hidden_global_offset_z
      - .offset:         400
        .size:           2
        .value_kind:     hidden_grid_dims
      - .offset:         456
        .size:           4
        .value_kind:     hidden_dynamic_lds_size
    .group_segment_fixed_size: 0
    .kernarg_segment_align: 8
    .kernarg_segment_size: 592
    .language:       OpenCL C
    .language_version:
      - 2
      - 0
    .max_flat_workgroup_size: 512
    .name:           _Z14gemm256_kernelILi0ELi512ELi1536EEv8GemmArgs
    .private_segment_fixed_size: 0
    .sgpr_count:     78
    .sgpr_spill_count: 0
    .symbol:         _Z14gemm256_kernelILi0ELi512ELi1536EEv8GemmArgs.kd
    .uniform_work_group_size: 1
    .uses_dynamic_stack: false
    .vgpr_count:     256
    .vgpr_spill_count: 0
    .wavefront_size: 64
  - .agpr_count:     0
    .args:
      - .offset:         0
        .size:           336
        .value_kind:     by_value
      - .offset:         336
        .size:           4
        .value_kind:     hidden_block_count_x
      - .offset:         340
        .size:           4
        .value_kind:     hidden_block_count_y
      - .offset:         344
        .size:           4
        .value_kind:     hidden_block_count_z
      - .offset:         348
        .size:           2
        .value_kind:     hidden_group_size_x
      - .offset:         350
        .size:           2
        .value_kind:     hidden_group_size_y
      - .offset:         352
        .size:           2
        .value_kind:     hidden_group_size_z
      - .offset:         354
        .size:           2
        .value_kind:     hidden_remainder_x
      - .offset:         356
        .size:           2
        .value_kind:     hidden_remainder_y
      - .offset:         358
        .size:           2
        .value_kind:     hidden_remainder_z
      - .offset:         376
        .size:           8
        .value_kind:     hidden_global_offset_x
      - .offset:         384
        .size:           8
        .value_kind:     hidden_global_offset_y
      - .offset:         392
        .size:           8
        .value_kind:     hidden_global_offset_z
      - .offset:         400
        .size:           2
        .value_kind:     hidden_grid_dims
      - .offset:         456
        .size:           4
        .value_kind:     hidden_dynamic_lds_size
    .group_segment_fixed_size: 0
    .kernarg_segment_align: 8
    .kernarg_segment_size: 592
    .language:       OpenCL C
    .language_version:
      - 2
      - 0
    .max_flat_workgroup_size: 512
    .name:           _Z14gemm256_kernelILi0ELi512ELi1024EEv8GemmArgs
    .private_segment_fixed_size: 0
    .sgpr_count:     78
    .sgpr_spill_count: 0
    .symbol:         _Z14gemm256_kernelILi0ELi512ELi1024EEv8GemmArgs.kd
    .uniform_work_group_size: 1
    .uses_dynamic_stack: false
    .vgpr_count:     256
    .vgpr_spill_count: 0
    .wavefront_size: 64
  - .agpr_count:     0
    .args:
      - .offset:         0
        .size:           336
        .value_kind:     by_value
      - .offset:         336
        .size:           4
        .value_kind:     hidden_block_count_x
      - .offset:         340
        .size:           4
        .value_kind:     hidden_block_count_y
      - .offset:         344
        .size:           4
        .value_kind:     hidden_block_count_z
      - .offset:         348
        .size:           2
        .value_kind:     hidden_group_size_x
      - .offset:         350
        .size:           2
        .value_kind:     hidden_group_size_y
      - .offset:         352
        .size:           2
        .value_kind:     hidden_group_size_z
      - .offset:         354
        .size:           2
        .value_kind:     hidden_remainder_x
      - .offset:         356
        .size:           2
        .value_kind:     hidden_remainder_y
      - .offset:         358
        .size:           2
        .value_kind:     hidden_remainder_z
      - .offset:         376
        .size:           8
        .value_kind:     hidden_global_offset_x
      - .offset:         384
        .size:           8
        .value_kind:     hidden_global_offset_y
      - .offset:         392
        .size:           8
        .value_kind:     hidden_global_offset_z
      - .offset:         400
        .size:           2
        .value_kind:     hidden_grid_dims
      - .offset:         456
        .size:           4
        .value_kind:     hidden_dynamic_lds_size
    .group_segment_fixed_size: 0
    .kernarg_segment_align: 8
    .kernarg_segment_size: 592
    .language:       OpenCL C
    .language_version:
      - 2
      - 0
    .max_flat_workgroup_size: 512
    .name:           _Z14gemm256_kernelILi1ELi512ELi512EEv8GemmArgs
    .private_segment_fixed_size: 0
    .sgpr_count:     81
    .sgpr_spill_count: 0
    .symbol:         _Z14gemm256_kernelILi1ELi512ELi512EEv8GemmArgs.kd
    .uniform_work_group_size: 1
    .uses_dynamic_stack: false
    .vgpr_count:     256
    .vgpr_spill_count: 0
    .wavefront_size: 64
  - .agpr_count:     0
    .args:
      - .offset:         0
        .size:           336
        .value_kind:     by_value
      - .offset:         336
        .size:           4
        .value_kind:     hidden_block_count_x
      - .offset:         340
        .size:           4
        .value_kind:     hidden_block_count_y
      - .offset:         344
        .size:           4
        .value_kind:     hidden_block_count_z
      - .offset:         348
        .size:           2
        .value_kind:     hidden_group_size_x
      - .offset:         350
        .size:           2
        .value_kind:     hidden_group_size_y
      - .offset:         352
        .size:           2
        .value_kind:     hidden_group_size_z
      - .offset:         354
        .size:           2
        .value_kind:     hidden_remainder_x
      - .offset:         356
        .size:           2
        .value_kind:     hidden_remainder_y
      - .offset:         358
        .size:           2
        .value_kind:     hidden_remainder_z
      - .offset:         376
        .size:           8
        .value_kind:     hidden_global_offset_x
      - .offset:         384
        .size:           8
        .value_kind:     hidden_global_offset_y
      - .offset:         392
        .size:           8
        .value_kind:     hidden_global_offset_z
      - .offset:         400
        .size:           2
        .value_kind:     hidden_grid_dims
      - .offset:         456
        .size:           4
        .value_kind:     hidden_dynamic_lds_size
    .group_segment_fixed_size: 0
    .kernarg_segment_align: 8
    .kernarg_segment_size: 592
    .language:       OpenCL C
    .language_version:
      - 2
      - 0
    .max_flat_workgroup_size: 512
    .name:           _Z14gemm256_kernelILi2ELi512ELi2048EEv8GemmArgs
    .private_segment_fixed_size: 0
    .sgpr_count:     68
    .sgpr_spill_count: 0
    .symbol:         _Z14gemm256_kernelILi2ELi512ELi2048EEv8GemmArgs.kd
    .uniform_work_group_size: 1
    .uses_dynamic_stack: false
    .vgpr_count:     254
    .vgpr_spill_count: 0
    .wavefront_size: 64
  - .agpr_count:     0
    .args:
      - .offset:         0
        .size:           336
        .value_kind:     by_value
      - .offset:         336
        .size:           4
        .value_kind:     hidden_block_count_x
      - .offset:         340
        .size:           4
        .value_kind:     hidden_block_count_y
      - .offset:         344
        .size:           4
        .value_kind:     hidden_block_count_z
      - .offset:         348
        .size:           2
        .value_kind:     hidden_group_size_x
      - .offset:         350
        .size:           2
        .value_kind:     hidden_group_size_y
      - .offset:         352
        .size:           2
        .value_kind:     hidden_group_size_z
      - .offset:         354
        .size:           2
        .value_kind:     hidden_remainder_x
      - .offset:         356
        .size:           2
        .value_kind:     hidden_remainder_y
      - .offset:         358
        .size:           2
        .value_kind:     hidden_remainder_z
      - .offset:         376
        .size:           8
        .value_kind:     hidden_global_offset_x
      - .offset:         384
        .size:           8
        .value_kind:     hidden_global_offset_y
      - .offset:         392
        .size:           8
        .value_kind:     hidden_global_offset_z
      - .offset:         400
        .size:           2
        .value_kind:     hidden_grid_dims
      - .offset:         456
        .size:           4
        .value_kind:     hidden_dynamic_lds_size
    .group_segment_fixed_size: 0
    .kernarg_segment_align: 8
    .kernarg_segment_size: 592
    .language:       OpenCL C
    .language_version:
      - 2
      - 0
    .max_flat_workgroup_size: 512
    .name:           _Z14gemm256_kernelILi1ELi2048ELi512EEv8GemmArgs
    .private_segment_fixed_size: 0
    .sgpr_count:     76
    .sgpr_spill_count: 0
    .symbol:         _Z14gemm256_kernelILi1ELi2048ELi512EEv8GemmArgs.kd
    .uniform_work_group_size: 1
    .uses_dynamic_stack: false
    .vgpr_count:     256
    .vgpr_spill_count: 0
    .wavefront_size: 64
  - .agpr_count:     0
    .args:
      - .offset:         0
        .size:           336
        .value_kind:     by_value
    .group_segment_fixed_size: 0
    .kernarg_segment_align: 8
    .kernarg_segment_size: 336
    .language:       OpenCL C
    .language_version:
      - 2
      - 0
    .max_flat_workgroup_size: 256
    .name:           _Z11gemm_kernelILi4EEv8GemmArgs
    .private_segment_fixed_size: 0
    .sgpr_count:     42
    .sgpr_spill_count: 0
    .symbol:         _Z11gemm_kernelILi4EEv8GemmArgs.kd
    .uniform_work_group_size: 1
    .uses_dynamic_stack: false
    .vgpr_count:     196
    .vgpr_spill_count: 0
    .wavefront_size: 64
  - .agpr_count:     0
    .args:
      - .offset:         0
        .size:           336
        .value_kind:     by_value
    .group_segment_fixed_size: 0
    .kernarg_segment_align: 8
    .kernarg_segment_size: 336
    .language:       OpenCL C
    .language_version:
      - 2
      - 0
    .max_flat_workgroup_size: 256
    .name:           _Z11gemm_kernelILi3EEv8GemmArgs
    .private_segment_fixed_size: 0
    .sgpr_count:     38
    .sgpr_spill_count: 0
    .symbol:         _Z11gemm_kernelILi3EEv8GemmArgs.kd
    .uniform_work_group_size: 1
    .uses_dynamic_stack: false
    .vgpr_count:     200
    .vgpr_spill_count: 0
    .wavefront_size: 64
